# attention tile B: score scaling packed too (7 v_pk_fma_f32 on renamed even-aligned temporaries + 1 scalar, was 15 v_fmamk_f32); bit-identical
# speedup vs baseline: 1.0042x; 1.0042x over previous
.LBB0_2723:
	v_cndmask_b32_e64 v219, v4, v219, s[8:9]
	v_mul_f32_e32 v4, 0xbe0293ee, v219
	v_mov_b32_e32 v24, v4
	v_pk_fma_f32 v[6:7], v[114:115], s[90:91], v[4:5] op_sel_hi:[1,0,0]
	v_fmamk_f32 v5, v128, 0x3e0293ee, v4
	s_waitcnt vmcnt(2)
	v_pk_fma_f32 v[8:9], v[116:117], s[90:91], v[4:5] op_sel_hi:[1,0,0]
	v_pk_fma_f32 v[10:11], v[118:119], s[90:91], v[4:5] op_sel_hi:[1,0,0]
	s_waitcnt vmcnt(1)
	v_pk_fma_f32 v[12:13], v[120:121], s[90:91], v[4:5] op_sel_hi:[1,0,0]
	v_pk_fma_f32 v[14:15], v[122:123], s[90:91], v[4:5] op_sel_hi:[1,0,0]
	v_pk_fma_f32 v[20:21], v[124:125], s[90:91], v[4:5] op_sel_hi:[1,0,0]
	v_pk_fma_f32 v[22:23], v[126:127], s[90:91], v[4:5] op_sel_hi:[1,0,0]
	v_fmac_f32_e32 v24, 0x3e0293ee, v129
	v_exp_f32_e32 v154, v6
	v_exp_f32_e32 v158, v7
	v_exp_f32_e32 v155, v8
	v_exp_f32_e32 v159, v9
	v_exp_f32_e32 v156, v10
	v_exp_f32_e32 v160, v11
	v_exp_f32_e32 v157, v12
	v_exp_f32_e32 v161, v13
	v_exp_f32_e32 v146, v14
	v_exp_f32_e32 v150, v15
	v_exp_f32_e32 v147, v20
	v_exp_f32_e32 v151, v21
	v_exp_f32_e32 v148, v22
	v_exp_f32_e32 v152, v23
	v_exp_f32_e32 v149, v5
	v_exp_f32_e32 v153, v24
	v_pk_fma_f32 v[144:145], v[98:99], s[0:1], v[4:5] op_sel_hi:[1,0,0]
	v_pk_fma_f32 v[140:141], v[100:101], s[0:1], v[4:5] op_sel_hi:[1,0,0]
	v_pk_fma_f32 v[138:139], v[102:103], s[0:1], v[4:5] op_sel_hi:[1,0,0]
	v_pk_fma_f32 v[132:133], v[104:105], s[0:1], v[4:5] op_sel_hi:[1,0,0]
	v_pk_fma_f32 v[130:131], v[106:107], s[0:1], v[4:5] op_sel_hi:[1,0,0]
	v_pk_fma_f32 v[142:143], v[108:109], s[0:1], v[4:5] op_sel_hi:[1,0,0]
	v_pk_fma_f32 v[136:137], v[110:111], s[0:1], v[4:5] op_sel_hi:[1,0,0]
	v_pk_fma_f32 v[134:135], v[112:113], s[0:1], v[4:5] op_sel_hi:[1,0,0]
	v_add_f32_e32 v4, v16, v17
	v_fmac_f32_e32 v4, v189, v216
	v_add_f32_e32 v216, v19, v32
	s_addk_i32 s86, 0x80
	s_add_i32 s2, s87, 2
	v_fmac_f32_e32 v216, v4, v220
	s_cmp_ge_u32 s2, s85
	s_waitcnt lgkmcnt(0)
	s_barrier
	s_cbranch_scc1 .LBB0_2725
	s_mov_b32 s90, s87
	v_mov_b32_e32 v189, v2
	s_branch .LBB0_2664
